# spatial: three key blocks of the max pass stay in registers (o accumulators and the idle pf/vf registers) so only four QK blocks are recomputed
# speedup vs baseline: 1.0333x; 1.0024x over previous
_Z9k_spatialPKDF16_S0_S0_PfPDF16_:
	s_load_dwordx4 s[4:7], s[0:1], 0x0
	s_load_dwordx2 s[10:11], s[0:1], 0x10
	s_mul_hi_i32 s9, s2, 0x3140
	s_mul_i32 s8, s2, 0x3140
	s_lshl_b64 s[8:9], s[8:9], 1
	v_and_b32_e32 v2, 7, v0
	v_lshrrev_b32_e32 v3, 3, v0
	v_lshlrev_b32_e32 v10, 4, v2
	v_lshl_or_b32 v4, v3, 7, v10
	v_add_u32_e32 v5, 0x1c00, v4
	v_add_u32_e32 v6, 0x3800, v4
	v_add_u32_e32 v7, 0x5400, v4
	v_lshrrev_b32_e32 v8, 1, v0
	v_and_b32_e32 v108, 31, v0
	v_and_b32_e32 v115, 0xe0, v8
	v_or_b32_e32 v109, v115, v108
	s_movk_i32 s3, 0xc5
	v_mov_b32_e32 v8, 0xc4
	v_cmp_gt_u32_e64 s[12:13], s3, v109
	v_bfe_u32 v1, v0, 5, 1
	v_lshlrev_b32_e32 v111, 4, v1
	s_nop 1
	v_cndmask_b32_e64 v110, v8, v109, s[12:13]
	v_lshl_or_b32 v9, v110, 7, v111
	s_movk_i32 s3, 0xe8
	v_cmp_gt_u32_e32 vcc, s3, v0
	v_or_b32_e32 v14, 0x6200, v10
	s_nop 1
	v_cndmask_b32_e32 v7, v14, v7, vcc
	s_waitcnt lgkmcnt(0)
	s_add_u32 s6, s6, s8
	s_addc_u32 s7, s7, s9
	s_add_u32 s10, s10, s8
	s_addc_u32 s11, s11, s9
	s_add_u32 s4, s4, s8
	s_addc_u32 s5, s5, s9
	global_load_dwordx4 v[18:21], v4, s[6:7] nt
	global_load_dwordx4 v[22:25], v4, s[10:11] nt
	global_load_dwordx4 v[26:29], v5, s[6:7] nt
	global_load_dwordx4 v[30:33], v5, s[10:11] nt
	global_load_dwordx4 v[34:37], v6, s[6:7] nt
	global_load_dwordx4 v[38:41], v6, s[10:11] nt
	global_load_dwordx4 v[42:45], v7, s[6:7] nt
	global_load_dwordx4 v[46:49], v7, s[10:11] nt
	global_load_dwordx4 v[74:77], v9, s[4:5] offset:0 nt
	global_load_dwordx4 v[78:81], v9, s[4:5] offset:32 nt
	global_load_dwordx4 v[82:85], v9, s[4:5] offset:64 nt
	global_load_dwordx4 v[86:89], v9, s[4:5] offset:96 nt
	s_movk_i32 s3, 0x90
	v_lshlrev_b32_e32 v11, 3, v2
	v_mul_u32_u24_e32 v16, 0x1c8, v11
	v_mad_u32_u24 v12, v3, s3, v10
	v_lshl_add_u32 v13, v3, 1, v16
	v_mad_u32_u24 v112, v108, s3, v111
	s_waitcnt vmcnt(11)
	ds_write_b128 v12, v[18:21] offset:0
	s_waitcnt vmcnt(10)
	ds_write_b16 v13, v22 offset:32256
	ds_write_b16_d16_hi v13, v22 offset:32712
	ds_write_b16 v13, v23 offset:33168
	ds_write_b16_d16_hi v13, v23 offset:33624
	ds_write_b16 v13, v24 offset:34080
	ds_write_b16_d16_hi v13, v24 offset:34536
	ds_write_b16 v13, v25 offset:34992
	ds_write_b16_d16_hi v13, v25 offset:35448
	s_waitcnt vmcnt(9)
	ds_write_b128 v12, v[26:29] offset:8064
	s_waitcnt vmcnt(8)
	ds_write_b16 v13, v30 offset:32368
	ds_write_b16_d16_hi v13, v30 offset:32824
	ds_write_b16 v13, v31 offset:33280
	ds_write_b16_d16_hi v13, v31 offset:33736
	ds_write_b16 v13, v32 offset:34192
	ds_write_b16_d16_hi v13, v32 offset:34648
	ds_write_b16 v13, v33 offset:35104
	ds_write_b16_d16_hi v13, v33 offset:35560
	s_waitcnt vmcnt(7)
	ds_write_b128 v12, v[34:37] offset:16128
	s_waitcnt vmcnt(6)
	ds_write_b16 v13, v38 offset:32480
	ds_write_b16_d16_hi v13, v38 offset:32936
	ds_write_b16 v13, v39 offset:33392
	ds_write_b16_d16_hi v13, v39 offset:33848
	ds_write_b16 v13, v40 offset:34304
	ds_write_b16_d16_hi v13, v40 offset:34760
	ds_write_b16 v13, v41 offset:35216
	ds_write_b16_d16_hi v13, v41 offset:35672
	s_waitcnt vmcnt(5)
	v_cndmask_b32_e32 v42, 0, v42, vcc
	v_cndmask_b32_e32 v43, 0, v43, vcc
	v_cndmask_b32_e32 v44, 0, v44, vcc
	v_cndmask_b32_e32 v45, 0, v45, vcc
	ds_write_b128 v12, v[42:45] offset:24192
	s_waitcnt vmcnt(4)
	v_cndmask_b32_e32 v46, 0, v46, vcc
	v_cndmask_b32_e32 v47, 0, v47, vcc
	v_cndmask_b32_e32 v48, 0, v48, vcc
	v_cndmask_b32_e32 v49, 0, v49, vcc
	ds_write_b16 v13, v46 offset:32592
	ds_write_b16_d16_hi v13, v46 offset:33048
	ds_write_b16 v13, v47 offset:33504
	ds_write_b16_d16_hi v13, v47 offset:33960
	ds_write_b16 v13, v48 offset:34416
	ds_write_b16_d16_hi v13, v48 offset:34872
	ds_write_b16 v13, v49 offset:35328
	ds_write_b16_d16_hi v13, v49 offset:35784
	s_load_dwordx2 s[8:9], s[0:1], 0x20
	s_load_dwordx2 s[10:11], s[0:1], 0x18
	s_mov_b32 s16, 0x3e38aa3b
	s_mov_b32 s17, 0xf149f2ca
	v_cmp_eq_u32_e64 s[14:15], 0, v1
	v_mul_u32_u24_e32 v113, 0x1c8, v108
	v_lshl_add_u32 v113, v1, 3, v113
	v_add_u32_e32 v113, 0x7e00, v113
	v_add_u32_e32 v114, 0x3900, v113
	v_mov_b32_e32 v106, s17
	s_waitcnt vmcnt(0) lgkmcnt(0)
	s_barrier
	ds_read_b128 v[66:69], v112 offset:0
	ds_read_b128 v[70:73], v112 offset:32
	s_waitcnt lgkmcnt(1)
	v_mfma_f32_32x32x16_f16 v[2:17], v[66:69], v[74:77], 0
	ds_read_b128 v[66:69], v112 offset:64
	s_waitcnt lgkmcnt(1)
	v_mfma_f32_32x32x16_f16 v[2:17], v[70:73], v[78:81], v[2:17]
	ds_read_b128 v[70:73], v112 offset:96
	s_waitcnt lgkmcnt(1)
	v_mfma_f32_32x32x16_f16 v[2:17], v[66:69], v[82:85], v[2:17]
	s_waitcnt lgkmcnt(0)
	v_mfma_f32_32x32x16_f16 v[2:17], v[70:73], v[86:89], v[2:17]
	ds_read_b128 v[66:69], v112 offset:4608
	ds_read_b128 v[70:73], v112 offset:4640
	s_waitcnt lgkmcnt(1)
	v_mfma_f32_32x32x16_f16 v[50:65], v[66:69], v[74:77], 0
	ds_read_b128 v[66:69], v112 offset:4672
	s_waitcnt lgkmcnt(1)
	v_mfma_f32_32x32x16_f16 v[50:65], v[70:73], v[78:81], v[50:65]
	ds_read_b128 v[70:73], v112 offset:4704
	s_waitcnt lgkmcnt(1)
	v_mfma_f32_32x32x16_f16 v[50:65], v[66:69], v[82:85], v[50:65]
	s_waitcnt lgkmcnt(0)
	v_mfma_f32_32x32x16_f16 v[50:65], v[70:73], v[86:89], v[50:65]
	v_max3_f32 v106, v106, v2, v3
	v_max3_f32 v106, v106, v4, v5
	v_max3_f32 v106, v106, v6, v7
	v_max3_f32 v106, v106, v8, v9
	v_max3_f32 v106, v106, v10, v11
	v_max3_f32 v106, v106, v12, v13
	v_max3_f32 v106, v106, v14, v15
	v_max3_f32 v106, v106, v16, v17
	ds_read_b128 v[66:69], v112 offset:9216
	ds_read_b128 v[70:73], v112 offset:9248
	s_waitcnt lgkmcnt(1)
	v_mfma_f32_32x32x16_f16 v[2:17], v[66:69], v[74:77], 0
	ds_read_b128 v[66:69], v112 offset:9280
	s_waitcnt lgkmcnt(1)
	v_mfma_f32_32x32x16_f16 v[2:17], v[70:73], v[78:81], v[2:17]
	ds_read_b128 v[70:73], v112 offset:9312
	s_waitcnt lgkmcnt(1)
	v_mfma_f32_32x32x16_f16 v[2:17], v[66:69], v[82:85], v[2:17]
	s_waitcnt lgkmcnt(0)
	v_mfma_f32_32x32x16_f16 v[2:17], v[70:73], v[86:89], v[2:17]
	v_max3_f32 v106, v106, v50, v51
	v_max3_f32 v106, v106, v52, v53
	v_max3_f32 v106, v106, v54, v55
	v_max3_f32 v106, v106, v56, v57
	v_max3_f32 v106, v106, v58, v59
	v_max3_f32 v106, v106, v60, v61
	v_max3_f32 v106, v106, v62, v63
	v_max3_f32 v106, v106, v64, v65
	ds_read_b128 v[66:69], v112 offset:13824
	ds_read_b128 v[70:73], v112 offset:13856
	s_waitcnt lgkmcnt(1)
	v_mfma_f32_32x32x16_f16 v[50:65], v[66:69], v[74:77], 0
	ds_read_b128 v[66:69], v112 offset:13888
	s_waitcnt lgkmcnt(1)
	v_mfma_f32_32x32x16_f16 v[50:65], v[70:73], v[78:81], v[50:65]
	ds_read_b128 v[70:73], v112 offset:13920
	s_waitcnt lgkmcnt(1)
	v_mfma_f32_32x32x16_f16 v[50:65], v[66:69], v[82:85], v[50:65]
	s_waitcnt lgkmcnt(0)
	v_mfma_f32_32x32x16_f16 v[50:65], v[70:73], v[86:89], v[50:65]
	v_max3_f32 v106, v106, v2, v3
	v_max3_f32 v106, v106, v4, v5
	v_max3_f32 v106, v106, v6, v7
	v_max3_f32 v106, v106, v8, v9
	v_max3_f32 v106, v106, v10, v11
	v_max3_f32 v106, v106, v12, v13
	v_max3_f32 v106, v106, v14, v15
	v_max3_f32 v106, v106, v16, v17
	ds_read_b128 v[66:69], v112 offset:18432
	ds_read_b128 v[70:73], v112 offset:18464
	s_waitcnt lgkmcnt(1)
	v_mfma_f32_32x32x16_f16 v[18:33], v[66:69], v[74:77], 0
	ds_read_b128 v[66:69], v112 offset:18496
	s_waitcnt lgkmcnt(1)
	v_mfma_f32_32x32x16_f16 v[18:33], v[70:73], v[78:81], v[18:33]
	ds_read_b128 v[70:73], v112 offset:18528
	s_waitcnt lgkmcnt(1)
	v_mfma_f32_32x32x16_f16 v[18:33], v[66:69], v[82:85], v[18:33]
	s_waitcnt lgkmcnt(0)
	v_mfma_f32_32x32x16_f16 v[18:33], v[70:73], v[86:89], v[18:33]
	v_max3_f32 v106, v106, v50, v51
	v_max3_f32 v106, v106, v52, v53
	v_max3_f32 v106, v106, v54, v55
	v_max3_f32 v106, v106, v56, v57
	v_max3_f32 v106, v106, v58, v59
	v_max3_f32 v106, v106, v60, v61
	v_max3_f32 v106, v106, v62, v63
	v_max3_f32 v106, v106, v64, v65
	ds_read_b128 v[66:69], v112 offset:23040
	ds_read_b128 v[70:73], v112 offset:23072
	s_waitcnt lgkmcnt(1)
	v_mfma_f32_32x32x16_f16 v[34:49], v[66:69], v[74:77], 0
	ds_read_b128 v[66:69], v112 offset:23104
	s_waitcnt lgkmcnt(1)
	v_mfma_f32_32x32x16_f16 v[34:49], v[70:73], v[78:81], v[34:49]
	ds_read_b128 v[70:73], v112 offset:23136
	s_waitcnt lgkmcnt(1)
	v_mfma_f32_32x32x16_f16 v[34:49], v[66:69], v[82:85], v[34:49]
	s_waitcnt lgkmcnt(0)
	v_mfma_f32_32x32x16_f16 v[34:49], v[70:73], v[86:89], v[34:49]
	v_max3_f32 v106, v106, v18, v19
	v_max3_f32 v106, v106, v20, v21
	v_max3_f32 v106, v106, v22, v23
	v_max3_f32 v106, v106, v24, v25
	v_max3_f32 v106, v106, v26, v27
	v_max3_f32 v106, v106, v28, v29
	v_max3_f32 v106, v106, v30, v31
	v_max3_f32 v106, v106, v32, v33
	ds_read_b128 v[66:69], v112 offset:27648
	ds_read_b128 v[70:73], v112 offset:27680
	s_waitcnt lgkmcnt(1)
	v_mfma_f32_32x32x16_f16 v[90:105], v[66:69], v[74:77], 0
	ds_read_b128 v[66:69], v112 offset:27712
	s_waitcnt lgkmcnt(1)
	v_mfma_f32_32x32x16_f16 v[90:105], v[70:73], v[78:81], v[90:105]
	ds_read_b128 v[70:73], v112 offset:27744
	s_waitcnt lgkmcnt(1)
	v_mfma_f32_32x32x16_f16 v[90:105], v[66:69], v[82:85], v[90:105]
	s_waitcnt lgkmcnt(0)
	v_mfma_f32_32x32x16_f16 v[90:105], v[70:73], v[86:89], v[90:105]
	v_max3_f32 v106, v106, v34, v35
	v_max3_f32 v106, v106, v36, v37
	v_max3_f32 v106, v106, v38, v39
	v_max3_f32 v106, v106, v40, v41
	v_max3_f32 v106, v106, v42, v43
	v_max3_f32 v106, v106, v44, v45
	v_max3_f32 v106, v106, v46, v47
	v_max3_f32 v106, v106, v48, v49
	s_nop 15
	s_nop 1
	v_mov_b32_e32 v94, s17
	v_mov_b32_e32 v95, s17
	v_mov_b32_e32 v96, s17
	v_mov_b32_e32 v97, s17
	v_mov_b32_e32 v98, s17
	v_mov_b32_e32 v99, s17
	v_mov_b32_e32 v100, s17
	v_mov_b32_e32 v101, s17
	v_mov_b32_e32 v102, s17
	v_mov_b32_e32 v103, s17
	v_mov_b32_e32 v104, s17
	v_mov_b32_e32 v105, s17
	v_mov_b32_e32 v120, s17
	v_cndmask_b32_e64 v91, v120, v91, s[14:15]
	v_cndmask_b32_e64 v92, v120, v92, s[14:15]
	v_cndmask_b32_e64 v93, v120, v93, s[14:15]
	v_max3_f32 v106, v106, v90, v91
	v_max3_f32 v106, v106, v92, v93
	v_max3_f32 v106, v106, v94, v95
	v_max3_f32 v106, v106, v96, v97
	v_max3_f32 v106, v106, v98, v99
	v_max3_f32 v106, v106, v100, v101
	v_max3_f32 v106, v106, v102, v103
	v_max3_f32 v106, v106, v104, v105
	v_mov_b32_e32 v120, v106
	v_mov_b32_e32 v121, v106
	s_nop 1
	v_permlane32_swap_b32_e32 v120, v121
	s_nop 1
	v_max3_f32 v106, v106, v120, v121
	v_mul_f32_e32 v106, s16, v106
	v_mov_b32_e32 v107, 0
	v_fma_f32 v120, v18, s16, -v106
	v_exp_f32_e32 v18, v120
	v_fma_f32 v121, v19, s16, -v106
	v_exp_f32_e32 v19, v121
	v_fma_f32 v122, v20, s16, -v106
	v_exp_f32_e32 v20, v122
	v_fma_f32 v123, v21, s16, -v106
	v_exp_f32_e32 v21, v123
	v_fma_f32 v120, v22, s16, -v106
	v_exp_f32_e32 v22, v120
	v_fma_f32 v121, v23, s16, -v106
	v_exp_f32_e32 v23, v121
	v_fma_f32 v122, v24, s16, -v106
	v_exp_f32_e32 v24, v122
	v_fma_f32 v123, v25, s16, -v106
	v_exp_f32_e32 v25, v123
	v_fma_f32 v120, v26, s16, -v106
	v_exp_f32_e32 v26, v120
	v_fma_f32 v121, v27, s16, -v106
	v_exp_f32_e32 v27, v121
	v_fma_f32 v122, v28, s16, -v106
	v_exp_f32_e32 v28, v122
	v_fma_f32 v123, v29, s16, -v106
	v_exp_f32_e32 v29, v123
	v_fma_f32 v120, v30, s16, -v106
	v_exp_f32_e32 v30, v120
	v_fma_f32 v121, v31, s16, -v106
	v_exp_f32_e32 v31, v121
	v_fma_f32 v122, v32, s16, -v106
	v_exp_f32_e32 v32, v122
	v_fma_f32 v123, v33, s16, -v106
	v_exp_f32_e32 v33, v123
	v_add_f32_e32 v107, v107, v18
	v_add_f32_e32 v107, v107, v19
	v_add_f32_e32 v107, v107, v20
	v_add_f32_e32 v107, v107, v21
	v_add_f32_e32 v107, v107, v22
	v_add_f32_e32 v107, v107, v23
	v_add_f32_e32 v107, v107, v24
	v_add_f32_e32 v107, v107, v25
	v_add_f32_e32 v107, v107, v26
	v_add_f32_e32 v107, v107, v27
	v_add_f32_e32 v107, v107, v28
	v_add_f32_e32 v107, v107, v29
	v_add_f32_e32 v107, v107, v30
	v_add_f32_e32 v107, v107, v31
	v_add_f32_e32 v107, v107, v32
	v_add_f32_e32 v107, v107, v33
	v_cvt_pk_f16_f32 v66, v18, v19
	v_cvt_pk_f16_f32 v67, v20, v21
	v_cvt_pk_f16_f32 v68, v22, v23
	v_cvt_pk_f16_f32 v69, v24, v25
	v_cvt_pk_f16_f32 v70, v26, v27
	v_cvt_pk_f16_f32 v71, v28, v29
	v_cvt_pk_f16_f32 v72, v30, v31
	v_cvt_pk_f16_f32 v73, v32, v33
	v_fma_f32 v120, v34, s16, -v106
	v_exp_f32_e32 v34, v120
	v_fma_f32 v121, v35, s16, -v106
	v_exp_f32_e32 v35, v121
	v_fma_f32 v122, v36, s16, -v106
	v_exp_f32_e32 v36, v122
	v_fma_f32 v123, v37, s16, -v106
	v_exp_f32_e32 v37, v123
	v_fma_f32 v120, v38, s16, -v106
	v_exp_f32_e32 v38, v120
	v_fma_f32 v121, v39, s16, -v106
	v_exp_f32_e32 v39, v121
	v_fma_f32 v122, v40, s16, -v106
	v_exp_f32_e32 v40, v122
	v_fma_f32 v123, v41, s16, -v106
	v_exp_f32_e32 v41, v123
	v_fma_f32 v120, v42, s16, -v106
	v_exp_f32_e32 v42, v120
	v_fma_f32 v121, v43, s16, -v106
	v_exp_f32_e32 v43, v121
	v_fma_f32 v122, v44, s16, -v106
	v_exp_f32_e32 v44, v122
	v_fma_f32 v123, v45, s16, -v106
	v_exp_f32_e32 v45, v123
	v_fma_f32 v120, v46, s16, -v106
	v_exp_f32_e32 v46, v120
	v_fma_f32 v121, v47, s16, -v106
	v_exp_f32_e32 v47, v121
	v_fma_f32 v122, v48, s16, -v106
	v_exp_f32_e32 v48, v122
	v_fma_f32 v123, v49, s16, -v106
	v_exp_f32_e32 v49, v123
	v_add_f32_e32 v107, v107, v34
	v_add_f32_e32 v107, v107, v35
	v_add_f32_e32 v107, v107, v36
	v_add_f32_e32 v107, v107, v37
	v_add_f32_e32 v107, v107, v38
	v_add_f32_e32 v107, v107, v39
	v_add_f32_e32 v107, v107, v40
	v_add_f32_e32 v107, v107, v41
	v_add_f32_e32 v107, v107, v42
	v_add_f32_e32 v107, v107, v43
	v_add_f32_e32 v107, v107, v44
	v_add_f32_e32 v107, v107, v45
	v_add_f32_e32 v107, v107, v46
	v_add_f32_e32 v107, v107, v47
	v_add_f32_e32 v107, v107, v48
	v_add_f32_e32 v107, v107, v49
	v_cvt_pk_f16_f32 v50, v34, v35
	v_cvt_pk_f16_f32 v51, v36, v37
	v_cvt_pk_f16_f32 v52, v38, v39
	v_cvt_pk_f16_f32 v53, v40, v41
	v_cvt_pk_f16_f32 v54, v42, v43
	v_cvt_pk_f16_f32 v55, v44, v45
	v_cvt_pk_f16_f32 v56, v46, v47
	v_cvt_pk_f16_f32 v57, v48, v49
	v_mov_b32_e32 v18, 0
	v_mov_b32_e32 v19, 0
	v_mov_b32_e32 v20, 0
	v_mov_b32_e32 v21, 0
	v_mov_b32_e32 v22, 0
	v_mov_b32_e32 v23, 0
	v_mov_b32_e32 v24, 0
	v_mov_b32_e32 v25, 0
	v_mov_b32_e32 v26, 0
	v_mov_b32_e32 v27, 0
	v_mov_b32_e32 v28, 0
	v_mov_b32_e32 v29, 0
	v_mov_b32_e32 v30, 0
	v_mov_b32_e32 v31, 0
	v_mov_b32_e32 v32, 0
	v_mov_b32_e32 v33, 0
	v_mov_b32_e32 v34, 0
	v_mov_b32_e32 v35, 0
	v_mov_b32_e32 v36, 0
	v_mov_b32_e32 v37, 0
	v_mov_b32_e32 v38, 0
	v_mov_b32_e32 v39, 0
	v_mov_b32_e32 v40, 0
	v_mov_b32_e32 v41, 0
	v_mov_b32_e32 v42, 0
	v_mov_b32_e32 v43, 0
	v_mov_b32_e32 v44, 0
	v_mov_b32_e32 v45, 0
	v_mov_b32_e32 v46, 0
	v_mov_b32_e32 v47, 0
	v_mov_b32_e32 v48, 0
	v_mov_b32_e32 v49, 0
	ds_read2_b64 v[58:61], v113 offset0:40 offset1:42
	ds_read2_b64 v[62:65], v114 offset0:40 offset1:42
	s_nop 1
	s_waitcnt lgkmcnt(1)
	v_mfma_f32_32x32x16_f16 v[18:33], v[58:61], v[50:53], v[18:33]
	ds_read2_b64 v[58:61], v113 offset0:44 offset1:46
	s_waitcnt lgkmcnt(1)
	v_mfma_f32_32x32x16_f16 v[34:49], v[62:65], v[50:53], v[34:49]
	ds_read2_b64 v[62:65], v114 offset0:44 offset1:46
	s_waitcnt lgkmcnt(1)
	v_mfma_f32_32x32x16_f16 v[18:33], v[58:61], v[54:57], v[18:33]
	s_waitcnt lgkmcnt(0)
	v_mfma_f32_32x32x16_f16 v[34:49], v[62:65], v[54:57], v[34:49]
	ds_read2_b64 v[58:61], v113 offset0:32 offset1:34
	ds_read2_b64 v[62:65], v114 offset0:32 offset1:34
	s_nop 1
	s_waitcnt lgkmcnt(1)
	v_mfma_f32_32x32x16_f16 v[18:33], v[58:61], v[66:69], v[18:33]
	ds_read2_b64 v[58:61], v113 offset0:36 offset1:38
	s_waitcnt lgkmcnt(1)
	v_mfma_f32_32x32x16_f16 v[34:49], v[62:65], v[66:69], v[34:49]
	ds_read2_b64 v[62:65], v114 offset0:36 offset1:38
	s_waitcnt lgkmcnt(1)
	v_mfma_f32_32x32x16_f16 v[18:33], v[58:61], v[70:73], v[18:33]
	s_waitcnt lgkmcnt(0)
	v_mfma_f32_32x32x16_f16 v[34:49], v[62:65], v[70:73], v[34:49]
	ds_read_b128 v[66:69], v112 offset:0
	ds_read_b128 v[70:73], v112 offset:32
	s_waitcnt lgkmcnt(1)
	v_mfma_f32_32x32x16_f16 v[2:17], v[66:69], v[74:77], 0
	ds_read_b128 v[66:69], v112 offset:64
	s_waitcnt lgkmcnt(1)
	v_mfma_f32_32x32x16_f16 v[2:17], v[70:73], v[78:81], v[2:17]
	ds_read_b128 v[70:73], v112 offset:96
	s_waitcnt lgkmcnt(1)
	v_mfma_f32_32x32x16_f16 v[2:17], v[66:69], v[82:85], v[2:17]
	s_waitcnt lgkmcnt(0)
	v_mfma_f32_32x32x16_f16 v[2:17], v[70:73], v[86:89], v[2:17]
	v_fma_f32 v120, v90, s16, -v106
	v_exp_f32_e32 v90, v120
	v_fma_f32 v121, v91, s16, -v106
	v_exp_f32_e32 v91, v121
	v_fma_f32 v122, v92, s16, -v106
	v_exp_f32_e32 v92, v122
	v_fma_f32 v123, v93, s16, -v106
	v_exp_f32_e32 v93, v123
	v_fma_f32 v120, v94, s16, -v106
	v_exp_f32_e32 v94, v120
	v_fma_f32 v121, v95, s16, -v106
	v_exp_f32_e32 v95, v121
	v_fma_f32 v122, v96, s16, -v106
	v_exp_f32_e32 v96, v122
	v_fma_f32 v123, v97, s16, -v106
	v_exp_f32_e32 v97, v123
	v_fma_f32 v120, v98, s16, -v106
	v_exp_f32_e32 v98, v120
	v_fma_f32 v121, v99, s16, -v106
	v_exp_f32_e32 v99, v121
	v_fma_f32 v122, v100, s16, -v106
	v_exp_f32_e32 v100, v122
	v_fma_f32 v123, v101, s16, -v106
	v_exp_f32_e32 v101, v123
	v_fma_f32 v120, v102, s16, -v106
	v_exp_f32_e32 v102, v120
	v_fma_f32 v121, v103, s16, -v106
	v_exp_f32_e32 v103, v121
	v_fma_f32 v122, v104, s16, -v106
	v_exp_f32_e32 v104, v122
	v_fma_f32 v123, v105, s16, -v106
	v_exp_f32_e32 v105, v123
	v_add_f32_e32 v107, v107, v90
	v_add_f32_e32 v107, v107, v91
	v_add_f32_e32 v107, v107, v92
	v_add_f32_e32 v107, v107, v93
	v_add_f32_e32 v107, v107, v94
	v_add_f32_e32 v107, v107, v95
	v_add_f32_e32 v107, v107, v96
	v_add_f32_e32 v107, v107, v97
	v_add_f32_e32 v107, v107, v98
	v_add_f32_e32 v107, v107, v99
	v_add_f32_e32 v107, v107, v100
	v_add_f32_e32 v107, v107, v101
	v_add_f32_e32 v107, v107, v102
	v_add_f32_e32 v107, v107, v103
	v_add_f32_e32 v107, v107, v104
	v_add_f32_e32 v107, v107, v105
	ds_read2_b64 v[58:61], v113 offset0:48 offset1:50
	ds_read2_b64 v[62:65], v114 offset0:48 offset1:50
	v_cvt_pk_f16_f32 v50, v90, v91
	v_cvt_pk_f16_f32 v51, v92, v93
	v_cvt_pk_f16_f32 v52, v94, v95
	v_cvt_pk_f16_f32 v53, v96, v97
	v_cvt_pk_f16_f32 v54, v98, v99
	v_cvt_pk_f16_f32 v55, v100, v101
	v_cvt_pk_f16_f32 v56, v102, v103
	v_cvt_pk_f16_f32 v57, v104, v105
	s_nop 1
	s_waitcnt lgkmcnt(1)
	v_mfma_f32_32x32x16_f16 v[18:33], v[58:61], v[50:53], v[18:33]
	ds_read2_b64 v[58:61], v113 offset0:52 offset1:54
	s_waitcnt lgkmcnt(1)
	v_mfma_f32_32x32x16_f16 v[34:49], v[62:65], v[50:53], v[34:49]
	ds_read2_b64 v[62:65], v114 offset0:52 offset1:54
	s_waitcnt lgkmcnt(1)
	v_mfma_f32_32x32x16_f16 v[18:33], v[58:61], v[54:57], v[18:33]
	s_waitcnt lgkmcnt(0)
	v_mfma_f32_32x32x16_f16 v[34:49], v[62:65], v[54:57], v[34:49]
	ds_read_b128 v[66:69], v112 offset:4608
	ds_read_b128 v[70:73], v112 offset:4640
	s_waitcnt lgkmcnt(1)
	v_mfma_f32_32x32x16_f16 v[90:105], v[66:69], v[74:77], 0
	ds_read_b128 v[66:69], v112 offset:4672
	s_waitcnt lgkmcnt(1)
	v_mfma_f32_32x32x16_f16 v[90:105], v[70:73], v[78:81], v[90:105]
	ds_read_b128 v[70:73], v112 offset:4704
	s_waitcnt lgkmcnt(1)
	v_mfma_f32_32x32x16_f16 v[90:105], v[66:69], v[82:85], v[90:105]
	s_waitcnt lgkmcnt(0)
	v_mfma_f32_32x32x16_f16 v[90:105], v[70:73], v[86:89], v[90:105]
	v_fma_f32 v120, v2, s16, -v106
	v_exp_f32_e32 v2, v120
	v_fma_f32 v121, v3, s16, -v106
	v_exp_f32_e32 v3, v121
	v_fma_f32 v122, v4, s16, -v106
	v_exp_f32_e32 v4, v122
	v_fma_f32 v123, v5, s16, -v106
	v_exp_f32_e32 v5, v123
	v_fma_f32 v120, v6, s16, -v106
	v_exp_f32_e32 v6, v120
	v_fma_f32 v121, v7, s16, -v106
	v_exp_f32_e32 v7, v121
	v_fma_f32 v122, v8, s16, -v106
	v_exp_f32_e32 v8, v122
	v_fma_f32 v123, v9, s16, -v106
	v_exp_f32_e32 v9, v123
	v_fma_f32 v120, v10, s16, -v106
	v_exp_f32_e32 v10, v120
	v_fma_f32 v121, v11, s16, -v106
	v_exp_f32_e32 v11, v121
	v_fma_f32 v122, v12, s16, -v106
	v_exp_f32_e32 v12, v122
	v_fma_f32 v123, v13, s16, -v106
	v_exp_f32_e32 v13, v123
	v_fma_f32 v120, v14, s16, -v106
	v_exp_f32_e32 v14, v120
	v_fma_f32 v121, v15, s16, -v106
	v_exp_f32_e32 v15, v121
	v_fma_f32 v122, v16, s16, -v106
	v_exp_f32_e32 v16, v122
	v_fma_f32 v123, v17, s16, -v106
	v_exp_f32_e32 v17, v123
	v_add_f32_e32 v107, v107, v2
	v_add_f32_e32 v107, v107, v3
	v_add_f32_e32 v107, v107, v4
	v_add_f32_e32 v107, v107, v5
	v_add_f32_e32 v107, v107, v6
	v_add_f32_e32 v107, v107, v7
	v_add_f32_e32 v107, v107, v8
	v_add_f32_e32 v107, v107, v9
	v_add_f32_e32 v107, v107, v10
	v_add_f32_e32 v107, v107, v11
	v_add_f32_e32 v107, v107, v12
	v_add_f32_e32 v107, v107, v13
	v_add_f32_e32 v107, v107, v14
	v_add_f32_e32 v107, v107, v15
	v_add_f32_e32 v107, v107, v16
	v_add_f32_e32 v107, v107, v17
	ds_read2_b64 v[58:61], v113 offset0:0 offset1:2
	ds_read2_b64 v[62:65], v114 offset0:0 offset1:2
	v_cvt_pk_f16_f32 v50, v2, v3
	v_cvt_pk_f16_f32 v51, v4, v5
	v_cvt_pk_f16_f32 v52, v6, v7
	v_cvt_pk_f16_f32 v53, v8, v9
	v_cvt_pk_f16_f32 v54, v10, v11
	v_cvt_pk_f16_f32 v55, v12, v13
	v_cvt_pk_f16_f32 v56, v14, v15
	v_cvt_pk_f16_f32 v57, v16, v17
	s_nop 1
	s_waitcnt lgkmcnt(1)
	v_mfma_f32_32x32x16_f16 v[18:33], v[58:61], v[50:53], v[18:33]
	ds_read2_b64 v[58:61], v113 offset0:4 offset1:6
	s_waitcnt lgkmcnt(1)
	v_mfma_f32_32x32x16_f16 v[34:49], v[62:65], v[50:53], v[34:49]
	ds_read2_b64 v[62:65], v114 offset0:4 offset1:6
	s_waitcnt lgkmcnt(1)
	v_mfma_f32_32x32x16_f16 v[18:33], v[58:61], v[54:57], v[18:33]
	s_waitcnt lgkmcnt(0)
	v_mfma_f32_32x32x16_f16 v[34:49], v[62:65], v[54:57], v[34:49]
	ds_read_b128 v[66:69], v112 offset:9216
	ds_read_b128 v[70:73], v112 offset:9248
	s_waitcnt lgkmcnt(1)
	v_mfma_f32_32x32x16_f16 v[2:17], v[66:69], v[74:77], 0
	ds_read_b128 v[66:69], v112 offset:9280
	s_waitcnt lgkmcnt(1)
	v_mfma_f32_32x32x16_f16 v[2:17], v[70:73], v[78:81], v[2:17]
	ds_read_b128 v[70:73], v112 offset:9312
	s_waitcnt lgkmcnt(1)
	v_mfma_f32_32x32x16_f16 v[2:17], v[66:69], v[82:85], v[2:17]
	s_waitcnt lgkmcnt(0)
	v_mfma_f32_32x32x16_f16 v[2:17], v[70:73], v[86:89], v[2:17]
	v_fma_f32 v120, v90, s16, -v106
	v_exp_f32_e32 v90, v120
	v_fma_f32 v121, v91, s16, -v106
	v_exp_f32_e32 v91, v121
	v_fma_f32 v122, v92, s16, -v106
	v_exp_f32_e32 v92, v122
	v_fma_f32 v123, v93, s16, -v106
	v_exp_f32_e32 v93, v123
	v_fma_f32 v120, v94, s16, -v106
	v_exp_f32_e32 v94, v120
	v_fma_f32 v121, v95, s16, -v106
	v_exp_f32_e32 v95, v121
	v_fma_f32 v122, v96, s16, -v106
	v_exp_f32_e32 v96, v122
	v_fma_f32 v123, v97, s16, -v106
	v_exp_f32_e32 v97, v123
	v_fma_f32 v120, v98, s16, -v106
	v_exp_f32_e32 v98, v120
	v_fma_f32 v121, v99, s16, -v106
	v_exp_f32_e32 v99, v121
	v_fma_f32 v122, v100, s16, -v106
	v_exp_f32_e32 v100, v122
	v_fma_f32 v123, v101, s16, -v106
	v_exp_f32_e32 v101, v123
	v_fma_f32 v120, v102, s16, -v106
	v_exp_f32_e32 v102, v120
	v_fma_f32 v121, v103, s16, -v106
	v_exp_f32_e32 v103, v121
	v_fma_f32 v122, v104, s16, -v106
	v_exp_f32_e32 v104, v122
	v_fma_f32 v123, v105, s16, -v106
	v_exp_f32_e32 v105, v123
	v_add_f32_e32 v107, v107, v90
	v_add_f32_e32 v107, v107, v91
	v_add_f32_e32 v107, v107, v92
	v_add_f32_e32 v107, v107, v93
	v_add_f32_e32 v107, v107, v94
	v_add_f32_e32 v107, v107, v95
	v_add_f32_e32 v107, v107, v96
	v_add_f32_e32 v107, v107, v97
	v_add_f32_e32 v107, v107, v98
	v_add_f32_e32 v107, v107, v99
	v_add_f32_e32 v107, v107, v100
	v_add_f32_e32 v107, v107, v101
	v_add_f32_e32 v107, v107, v102
	v_add_f32_e32 v107, v107, v103
	v_add_f32_e32 v107, v107, v104
	v_add_f32_e32 v107, v107, v105
	ds_read2_b64 v[58:61], v113 offset0:8 offset1:10
	ds_read2_b64 v[62:65], v114 offset0:8 offset1:10
	v_cvt_pk_f16_f32 v50, v90, v91
	v_cvt_pk_f16_f32 v51, v92, v93
	v_cvt_pk_f16_f32 v52, v94, v95
	v_cvt_pk_f16_f32 v53, v96, v97
	v_cvt_pk_f16_f32 v54, v98, v99
	v_cvt_pk_f16_f32 v55, v100, v101
	v_cvt_pk_f16_f32 v56, v102, v103
	v_cvt_pk_f16_f32 v57, v104, v105
	s_nop 1
	s_waitcnt lgkmcnt(1)
	v_mfma_f32_32x32x16_f16 v[18:33], v[58:61], v[50:53], v[18:33]
	ds_read2_b64 v[58:61], v113 offset0:12 offset1:14
	s_waitcnt lgkmcnt(1)
	v_mfma_f32_32x32x16_f16 v[34:49], v[62:65], v[50:53], v[34:49]
	ds_read2_b64 v[62:65], v114 offset0:12 offset1:14
	s_waitcnt lgkmcnt(1)
	v_mfma_f32_32x32x16_f16 v[18:33], v[58:61], v[54:57], v[18:33]
	s_waitcnt lgkmcnt(0)
	v_mfma_f32_32x32x16_f16 v[34:49], v[62:65], v[54:57], v[34:49]
	ds_read_b128 v[66:69], v112 offset:13824
	ds_read_b128 v[70:73], v112 offset:13856
	s_waitcnt lgkmcnt(1)
	v_mfma_f32_32x32x16_f16 v[90:105], v[66:69], v[74:77], 0
	ds_read_b128 v[66:69], v112 offset:13888
	s_waitcnt lgkmcnt(1)
	v_mfma_f32_32x32x16_f16 v[90:105], v[70:73], v[78:81], v[90:105]
	ds_read_b128 v[70:73], v112 offset:13920
	s_waitcnt lgkmcnt(1)
	v_mfma_f32_32x32x16_f16 v[90:105], v[66:69], v[82:85], v[90:105]
	s_waitcnt lgkmcnt(0)
	v_mfma_f32_32x32x16_f16 v[90:105], v[70:73], v[86:89], v[90:105]
	v_fma_f32 v120, v2, s16, -v106
	v_exp_f32_e32 v2, v120
	v_fma_f32 v121, v3, s16, -v106
	v_exp_f32_e32 v3, v121
	v_fma_f32 v122, v4, s16, -v106
	v_exp_f32_e32 v4, v122
	v_fma_f32 v123, v5, s16, -v106
	v_exp_f32_e32 v5, v123
	v_fma_f32 v120, v6, s16, -v106
	v_exp_f32_e32 v6, v120
	v_fma_f32 v121, v7, s16, -v106
	v_exp_f32_e32 v7, v121
	v_fma_f32 v122, v8, s16, -v106
	v_exp_f32_e32 v8, v122
	v_fma_f32 v123, v9, s16, -v106
	v_exp_f32_e32 v9, v123
	v_fma_f32 v120, v10, s16, -v106
	v_exp_f32_e32 v10, v120
	v_fma_f32 v121, v11, s16, -v106
	v_exp_f32_e32 v11, v121
	v_fma_f32 v122, v12, s16, -v106
	v_exp_f32_e32 v12, v122
	v_fma_f32 v123, v13, s16, -v106
	v_exp_f32_e32 v13, v123
	v_fma_f32 v120, v14, s16, -v106
	v_exp_f32_e32 v14, v120
	v_fma_f32 v121, v15, s16, -v106
	v_exp_f32_e32 v15, v121
	v_fma_f32 v122, v16, s16, -v106
	v_exp_f32_e32 v16, v122
	v_fma_f32 v123, v17, s16, -v106
	v_exp_f32_e32 v17, v123
	v_add_f32_e32 v107, v107, v2
	v_add_f32_e32 v107, v107, v3
	v_add_f32_e32 v107, v107, v4
	v_add_f32_e32 v107, v107, v5
	v_add_f32_e32 v107, v107, v6
	v_add_f32_e32 v107, v107, v7
	v_add_f32_e32 v107, v107, v8
	v_add_f32_e32 v107, v107, v9
	v_add_f32_e32 v107, v107, v10
	v_add_f32_e32 v107, v107, v11
	v_add_f32_e32 v107, v107, v12
	v_add_f32_e32 v107, v107, v13
	v_add_f32_e32 v107, v107, v14
	v_add_f32_e32 v107, v107, v15
	v_add_f32_e32 v107, v107, v16
	v_add_f32_e32 v107, v107, v17
	ds_read2_b64 v[58:61], v113 offset0:16 offset1:18
	ds_read2_b64 v[62:65], v114 offset0:16 offset1:18
	v_cvt_pk_f16_f32 v50, v2, v3
	v_cvt_pk_f16_f32 v51, v4, v5
	v_cvt_pk_f16_f32 v52, v6, v7
	v_cvt_pk_f16_f32 v53, v8, v9
	v_cvt_pk_f16_f32 v54, v10, v11
	v_cvt_pk_f16_f32 v55, v12, v13
	v_cvt_pk_f16_f32 v56, v14, v15
	v_cvt_pk_f16_f32 v57, v16, v17
	s_nop 1
	s_waitcnt lgkmcnt(1)
	v_mfma_f32_32x32x16_f16 v[18:33], v[58:61], v[50:53], v[18:33]
	ds_read2_b64 v[58:61], v113 offset0:20 offset1:22
	s_waitcnt lgkmcnt(1)
	v_mfma_f32_32x32x16_f16 v[34:49], v[62:65], v[50:53], v[34:49]
	ds_read2_b64 v[62:65], v114 offset0:20 offset1:22
	s_waitcnt lgkmcnt(1)
	v_mfma_f32_32x32x16_f16 v[18:33], v[58:61], v[54:57], v[18:33]
	s_waitcnt lgkmcnt(0)
	v_mfma_f32_32x32x16_f16 v[34:49], v[62:65], v[54:57], v[34:49]
	s_nop 15
	s_nop 1
	v_fma_f32 v120, v90, s16, -v106
	v_exp_f32_e32 v90, v120
	v_fma_f32 v121, v91, s16, -v106
	v_exp_f32_e32 v91, v121
	v_fma_f32 v122, v92, s16, -v106
	v_exp_f32_e32 v92, v122
	v_fma_f32 v123, v93, s16, -v106
	v_exp_f32_e32 v93, v123
	v_fma_f32 v120, v94, s16, -v106
	v_exp_f32_e32 v94, v120
	v_fma_f32 v121, v95, s16, -v106
	v_exp_f32_e32 v95, v121
	v_fma_f32 v122, v96, s16, -v106
	v_exp_f32_e32 v96, v122
	v_fma_f32 v123, v97, s16, -v106
	v_exp_f32_e32 v97, v123
	v_fma_f32 v120, v98, s16, -v106
	v_exp_f32_e32 v98, v120
	v_fma_f32 v121, v99, s16, -v106
	v_exp_f32_e32 v99, v121
	v_fma_f32 v122, v100, s16, -v106
	v_exp_f32_e32 v100, v122
	v_fma_f32 v123, v101, s16, -v106
	v_exp_f32_e32 v101, v123
	v_fma_f32 v120, v102, s16, -v106
	v_exp_f32_e32 v102, v120
	v_fma_f32 v121, v103, s16, -v106
	v_exp_f32_e32 v103, v121
	v_fma_f32 v122, v104, s16, -v106
	v_exp_f32_e32 v104, v122
	v_fma_f32 v123, v105, s16, -v106
	v_exp_f32_e32 v105, v123
	v_add_f32_e32 v107, v107, v90
	v_add_f32_e32 v107, v107, v91
	v_add_f32_e32 v107, v107, v92
	v_add_f32_e32 v107, v107, v93
	v_add_f32_e32 v107, v107, v94
	v_add_f32_e32 v107, v107, v95
	v_add_f32_e32 v107, v107, v96
	v_add_f32_e32 v107, v107, v97
	v_add_f32_e32 v107, v107, v98
	v_add_f32_e32 v107, v107, v99
	v_add_f32_e32 v107, v107, v100
	v_add_f32_e32 v107, v107, v101
	v_add_f32_e32 v107, v107, v102
	v_add_f32_e32 v107, v107, v103
	v_add_f32_e32 v107, v107, v104
	v_add_f32_e32 v107, v107, v105
	ds_read2_b64 v[58:61], v113 offset0:24 offset1:26
	ds_read2_b64 v[62:65], v114 offset0:24 offset1:26
	v_cvt_pk_f16_f32 v50, v90, v91
	v_cvt_pk_f16_f32 v51, v92, v93
	v_cvt_pk_f16_f32 v52, v94, v95
	v_cvt_pk_f16_f32 v53, v96, v97
	v_cvt_pk_f16_f32 v54, v98, v99
	v_cvt_pk_f16_f32 v55, v100, v101
	v_cvt_pk_f16_f32 v56, v102, v103
	v_cvt_pk_f16_f32 v57, v104, v105
	s_nop 1
	s_waitcnt lgkmcnt(1)
	v_mfma_f32_32x32x16_f16 v[18:33], v[58:61], v[50:53], v[18:33]
	ds_read2_b64 v[58:61], v113 offset0:28 offset1:30
	s_waitcnt lgkmcnt(1)
	v_mfma_f32_32x32x16_f16 v[34:49], v[62:65], v[50:53], v[34:49]
	ds_read2_b64 v[62:65], v114 offset0:28 offset1:30
	s_waitcnt lgkmcnt(1)
	v_mfma_f32_32x32x16_f16 v[18:33], v[58:61], v[54:57], v[18:33]
	s_waitcnt lgkmcnt(0)
	v_mfma_f32_32x32x16_f16 v[34:49], v[62:65], v[54:57], v[34:49]
	v_mov_b32_e32 v120, v107
	v_mov_b32_e32 v121, v107
	s_nop 1
	v_permlane32_swap_b32_e32 v120, v121
	s_nop 1
	v_add_f32_e32 v107, v120, v121
	v_log_f32_e32 v122, v107
	v_rcp_f32_e32 v123, v107
	s_nop 0
	v_add_f32_e32 v122, v122, v106
	v_fma_f32 v124, -v107, v123, 2.0
	v_mul_f32_e32 v123, v123, v124
	v_lshlrev_b32_e32 v125, 2, v109
	s_mov_b64 s[18:19], exec
	s_and_b64 exec, exec, s[14:15]
	ds_write_b32 v125, v122 offset:61440
	s_mov_b64 exec, s[18:19]
	s_mul_i32 s20, s2, 0x493
	s_lshr_b32 s20, s20, 16
	s_mul_i32 s21, s20, 56
	s_sub_u32 s21, s2, s21
	s_mul_i32 s22, s21, 0x2493
	s_lshr_b32 s22, s22, 16
	s_mul_i32 s23, s22, 7
	s_sub_u32 s23, s21, s23
	s_mul_i32 s24, s23, 0xc5
	s_lshl_b32 s24, s24, 13
	s_lshl_b32 s25, s22, 10
	s_add_u32 s24, s24, s25
	s_lshl_b32 s25, s20, 7
	s_add_u32 s24, s24, s25
	v_lshlrev_b32_e32 v125, 13, v110
	v_add3_u32 v125, v125, s24, v111
	s_nop 15
	s_waitcnt lgkmcnt(0)
	v_mul_f32_e32 v18, v18, v123
	v_mul_f32_e32 v19, v19, v123
	v_mul_f32_e32 v20, v20, v123
	v_mul_f32_e32 v21, v21, v123
	v_mul_f32_e32 v22, v22, v123
	v_mul_f32_e32 v23, v23, v123
	v_mul_f32_e32 v24, v24, v123
	v_mul_f32_e32 v25, v25, v123
	v_cvt_pk_f16_f32 v50, v18, v19
	v_cvt_pk_f16_f32 v51, v20, v21
	v_cvt_pk_f16_f32 v52, v22, v23
	v_cvt_pk_f16_f32 v53, v24, v25
	s_nop 1
	v_permlane32_swap_b32_e32 v50, v52
	v_permlane32_swap_b32_e32 v51, v53
	s_nop 1
	s_and_b64 exec, exec, s[12:13]
	global_store_dwordx4 v125, v[50:53], s[8:9] offset:0
	s_mov_b64 exec, s[18:19]
	s_nop 1
	v_mul_f32_e32 v26, v26, v123
	v_mul_f32_e32 v27, v27, v123
	v_mul_f32_e32 v28, v28, v123
	v_mul_f32_e32 v29, v29, v123
	v_mul_f32_e32 v30, v30, v123
	v_mul_f32_e32 v31, v31, v123
	v_mul_f32_e32 v32, v32, v123
	v_mul_f32_e32 v33, v33, v123
	v_cvt_pk_f16_f32 v54, v26, v27
	v_cvt_pk_f16_f32 v55, v28, v29
	v_cvt_pk_f16_f32 v56, v30, v31
	v_cvt_pk_f16_f32 v57, v32, v33
	s_nop 1
	v_permlane32_swap_b32_e32 v54, v56
	v_permlane32_swap_b32_e32 v55, v57
	s_nop 1
	s_and_b64 exec, exec, s[12:13]
	global_store_dwordx4 v125, v[54:57], s[8:9] offset:32
	s_mov_b64 exec, s[18:19]
	s_nop 1
	v_mul_f32_e32 v34, v34, v123
	v_mul_f32_e32 v35, v35, v123
	v_mul_f32_e32 v36, v36, v123
	v_mul_f32_e32 v37, v37, v123
	v_mul_f32_e32 v38, v38, v123
	v_mul_f32_e32 v39, v39, v123
	v_mul_f32_e32 v40, v40, v123
	v_mul_f32_e32 v41, v41, v123
	v_cvt_pk_f16_f32 v50, v34, v35
	v_cvt_pk_f16_f32 v51, v36, v37
	v_cvt_pk_f16_f32 v52, v38, v39
	v_cvt_pk_f16_f32 v53, v40, v41
	s_nop 1
	v_permlane32_swap_b32_e32 v50, v52
	v_permlane32_swap_b32_e32 v51, v53
	s_nop 1
	s_and_b64 exec, exec, s[12:13]
	global_store_dwordx4 v125, v[50:53], s[8:9] offset:64
	s_mov_b64 exec, s[18:19]
	s_nop 1
	v_mul_f32_e32 v42, v42, v123
	v_mul_f32_e32 v43, v43, v123
	v_mul_f32_e32 v44, v44, v123
	v_mul_f32_e32 v45, v45, v123
	v_mul_f32_e32 v46, v46, v123
	v_mul_f32_e32 v47, v47, v123
	v_mul_f32_e32 v48, v48, v123
	v_mul_f32_e32 v49, v49, v123
	v_cvt_pk_f16_f32 v54, v42, v43
	v_cvt_pk_f16_f32 v55, v44, v45
	v_cvt_pk_f16_f32 v56, v46, v47
	v_cvt_pk_f16_f32 v57, v48, v49
	s_nop 1
	v_permlane32_swap_b32_e32 v54, v56
	v_permlane32_swap_b32_e32 v55, v57
	s_nop 1
	s_and_b64 exec, exec, s[12:13]
	global_store_dwordx4 v125, v[54:57], s[8:9] offset:96
	s_mov_b64 exec, s[18:19]
	s_nop 1
	s_waitcnt lgkmcnt(0)
	s_barrier
	v_lshl_add_u32 v120, v115, 2, v111
	ds_read_b128 v[90:93], v120 offset:61440
	ds_read_b128 v[94:97], v120 offset:61472
	ds_read_b128 v[98:101], v120 offset:61504
	ds_read_b128 v[102:105], v120 offset:61536
	v_lshl_or_b32 v121, v1, 2, v115
	v_mul_u32_u24_e32 v121, 0xc5, v121
	v_add_lshl_u32 v116, v121, v108, 2
	v_add_u32_e32 v117, 0x18a0, v116
	v_add_u32_e32 v118, 0x3140, v116
	v_add_u32_e32 v119, 0x49e0, v116
	s_mul_hi_u32 s21, s2, 0x25e64
	s_mul_i32 s20, s2, 0x25e64
	s_add_u32 s10, s10, s20
	s_addc_u32 s11, s11, s21
	v_cmp_gt_u32_e64 s[22:23], 5, v108
	s_nop 0
	v_readfirstlane_b32 s26, v115
	s_cmp_eq_u32 s26, 0xc0
	s_cbranch_scc1 .Lsp_wave6
	ds_read_b128 v[66:69], v112 offset:0
	ds_read_b128 v[70:73], v112 offset:32
	s_waitcnt lgkmcnt(1)
	v_mfma_f32_32x32x16_f16 v[2:17], v[74:77], v[66:69], 0
	ds_read_b128 v[66:69], v112 offset:64
	s_waitcnt lgkmcnt(1)
	v_mfma_f32_32x32x16_f16 v[2:17], v[78:81], v[70:73], v[2:17]
	ds_read_b128 v[70:73], v112 offset:96
	s_waitcnt lgkmcnt(1)
	v_mfma_f32_32x32x16_f16 v[2:17], v[82:85], v[66:69], v[2:17]
	s_waitcnt lgkmcnt(0)
	v_mfma_f32_32x32x16_f16 v[2:17], v[86:89], v[70:73], v[2:17]
	s_waitcnt lgkmcnt(0)
	ds_read_b128 v[66:69], v112 offset:4608
	ds_read_b128 v[70:73], v112 offset:4640
	s_waitcnt lgkmcnt(1)
	v_mfma_f32_32x32x16_f16 v[18:33], v[74:77], v[66:69], 0
	ds_read_b128 v[66:69], v112 offset:4672
	s_waitcnt lgkmcnt(1)
	v_mfma_f32_32x32x16_f16 v[18:33], v[78:81], v[70:73], v[18:33]
	ds_read_b128 v[70:73], v112 offset:4704
	s_waitcnt lgkmcnt(1)
	v_mfma_f32_32x32x16_f16 v[18:33], v[82:85], v[66:69], v[18:33]
	s_waitcnt lgkmcnt(0)
	v_mfma_f32_32x32x16_f16 v[18:33], v[86:89], v[70:73], v[18:33]
	v_fma_f32 v120, v2, s16, -v90
	v_exp_f32_e32 v2, v120
	v_fma_f32 v121, v3, s16, -v91
	v_exp_f32_e32 v3, v121
	v_fma_f32 v122, v4, s16, -v92
	v_exp_f32_e32 v4, v122
	v_fma_f32 v123, v5, s16, -v93
	v_exp_f32_e32 v5, v123
	v_fma_f32 v120, v6, s16, -v94
	v_exp_f32_e32 v6, v120
	v_fma_f32 v121, v7, s16, -v95
	v_exp_f32_e32 v7, v121
	v_fma_f32 v122, v8, s16, -v96
	v_exp_f32_e32 v8, v122
	v_fma_f32 v123, v9, s16, -v97
	v_exp_f32_e32 v9, v123
	v_fma_f32 v120, v10, s16, -v98
	v_exp_f32_e32 v10, v120
	v_fma_f32 v121, v11, s16, -v99
	v_exp_f32_e32 v11, v121
	v_fma_f32 v122, v12, s16, -v100
	v_exp_f32_e32 v12, v122
	v_fma_f32 v123, v13, s16, -v101
	v_exp_f32_e32 v13, v123
	v_fma_f32 v120, v14, s16, -v102
	v_exp_f32_e32 v14, v120
	v_fma_f32 v121, v15, s16, -v103
	v_exp_f32_e32 v15, v121
	v_fma_f32 v122, v16, s16, -v104
	v_exp_f32_e32 v16, v122
	v_fma_f32 v123, v17, s16, -v105
	v_exp_f32_e32 v17, v123
	global_store_dword v116, v2, s[10:11] offset:0
	global_store_dword v116, v3, s[10:11] offset:788
	global_store_dword v116, v4, s[10:11] offset:1576
	global_store_dword v116, v5, s[10:11] offset:2364
	global_store_dword v117, v6, s[10:11] offset:0
	global_store_dword v117, v7, s[10:11] offset:788
	global_store_dword v117, v8, s[10:11] offset:1576
	global_store_dword v117, v9, s[10:11] offset:2364
	global_store_dword v118, v10, s[10:11] offset:0
	global_store_dword v118, v11, s[10:11] offset:788
	global_store_dword v118, v12, s[10:11] offset:1576
	global_store_dword v118, v13, s[10:11] offset:2364
	global_store_dword v119, v14, s[10:11] offset:0
	global_store_dword v119, v15, s[10:11] offset:788
	global_store_dword v119, v16, s[10:11] offset:1576
	global_store_dword v119, v17, s[10:11] offset:2364
	ds_read_b128 v[66:69], v112 offset:9216
	ds_read_b128 v[70:73], v112 offset:9248
	s_waitcnt lgkmcnt(1)
	v_mfma_f32_32x32x16_f16 v[2:17], v[74:77], v[66:69], 0
	ds_read_b128 v[66:69], v112 offset:9280
	s_waitcnt lgkmcnt(1)
	v_mfma_f32_32x32x16_f16 v[2:17], v[78:81], v[70:73], v[2:17]
	ds_read_b128 v[70:73], v112 offset:9312
	s_waitcnt lgkmcnt(1)
	v_mfma_f32_32x32x16_f16 v[2:17], v[82:85], v[66:69], v[2:17]
	s_waitcnt lgkmcnt(0)
	v_mfma_f32_32x32x16_f16 v[2:17], v[86:89], v[70:73], v[2:17]
	v_fma_f32 v120, v18, s16, -v90
	v_exp_f32_e32 v18, v120
	v_fma_f32 v121, v19, s16, -v91
	v_exp_f32_e32 v19, v121
	v_fma_f32 v122, v20, s16, -v92
	v_exp_f32_e32 v20, v122
	v_fma_f32 v123, v21, s16, -v93
	v_exp_f32_e32 v21, v123
	v_fma_f32 v120, v22, s16, -v94
	v_exp_f32_e32 v22, v120
	v_fma_f32 v121, v23, s16, -v95
	v_exp_f32_e32 v23, v121
	v_fma_f32 v122, v24, s16, -v96
	v_exp_f32_e32 v24, v122
	v_fma_f32 v123, v25, s16, -v97
	v_exp_f32_e32 v25, v123
	v_fma_f32 v120, v26, s16, -v98
	v_exp_f32_e32 v26, v120
	v_fma_f32 v121, v27, s16, -v99
	v_exp_f32_e32 v27, v121
	v_fma_f32 v122, v28, s16, -v100
	v_exp_f32_e32 v28, v122
	v_fma_f32 v123, v29, s16, -v101
	v_exp_f32_e32 v29, v123
	v_fma_f32 v120, v30, s16, -v102
	v_exp_f32_e32 v30, v120
	v_fma_f32 v121, v31, s16, -v103
	v_exp_f32_e32 v31, v121
	v_fma_f32 v122, v32, s16, -v104
	v_exp_f32_e32 v32, v122
	v_fma_f32 v123, v33, s16, -v105
	v_exp_f32_e32 v33, v123
	global_store_dword v116, v18, s[10:11] offset:128
	global_store_dword v116, v19, s[10:11] offset:916
	global_store_dword v116, v20, s[10:11] offset:1704
	global_store_dword v116, v21, s[10:11] offset:2492
	global_store_dword v117, v22, s[10:11] offset:128
	global_store_dword v117, v23, s[10:11] offset:916
	global_store_dword v117, v24, s[10:11] offset:1704
	global_store_dword v117, v25, s[10:11] offset:2492
	global_store_dword v118, v26, s[10:11] offset:128
	global_store_dword v118, v27, s[10:11] offset:916
	global_store_dword v118, v28, s[10:11] offset:1704
	global_store_dword v118, v29, s[10:11] offset:2492
	global_store_dword v119, v30, s[10:11] offset:128
	global_store_dword v119, v31, s[10:11] offset:916
	global_store_dword v119, v32, s[10:11] offset:1704
	global_store_dword v119, v33, s[10:11] offset:2492
	ds_read_b128 v[66:69], v112 offset:13824
	ds_read_b128 v[70:73], v112 offset:13856
	s_waitcnt lgkmcnt(1)
	v_mfma_f32_32x32x16_f16 v[18:33], v[74:77], v[66:69], 0
	ds_read_b128 v[66:69], v112 offset:13888
	s_waitcnt lgkmcnt(1)
	v_mfma_f32_32x32x16_f16 v[18:33], v[78:81], v[70:73], v[18:33]
	ds_read_b128 v[70:73], v112 offset:13920
	s_waitcnt lgkmcnt(1)
	v_mfma_f32_32x32x16_f16 v[18:33], v[82:85], v[66:69], v[18:33]
	s_waitcnt lgkmcnt(0)
	v_mfma_f32_32x32x16_f16 v[18:33], v[86:89], v[70:73], v[18:33]
	v_fma_f32 v120, v2, s16, -v90
	v_exp_f32_e32 v2, v120
	v_fma_f32 v121, v3, s16, -v91
	v_exp_f32_e32 v3, v121
	v_fma_f32 v122, v4, s16, -v92
	v_exp_f32_e32 v4, v122
	v_fma_f32 v123, v5, s16, -v93
	v_exp_f32_e32 v5, v123
	v_fma_f32 v120, v6, s16, -v94
	v_exp_f32_e32 v6, v120
	v_fma_f32 v121, v7, s16, -v95
	v_exp_f32_e32 v7, v121
	v_fma_f32 v122, v8, s16, -v96
	v_exp_f32_e32 v8, v122
	v_fma_f32 v123, v9, s16, -v97
	v_exp_f32_e32 v9, v123
	v_fma_f32 v120, v10, s16, -v98
	v_exp_f32_e32 v10, v120
	v_fma_f32 v121, v11, s16, -v99
	v_exp_f32_e32 v11, v121
	v_fma_f32 v122, v12, s16, -v100
	v_exp_f32_e32 v12, v122
	v_fma_f32 v123, v13, s16, -v101
	v_exp_f32_e32 v13, v123
	v_fma_f32 v120, v14, s16, -v102
	v_exp_f32_e32 v14, v120
	v_fma_f32 v121, v15, s16, -v103
	v_exp_f32_e32 v15, v121
	v_fma_f32 v122, v16, s16, -v104
	v_exp_f32_e32 v16, v122
	v_fma_f32 v123, v17, s16, -v105
	v_exp_f32_e32 v17, v123
	global_store_dword v116, v2, s[10:11] offset:256
	global_store_dword v116, v3, s[10:11] offset:1044
	global_store_dword v116, v4, s[10:11] offset:1832
	global_store_dword v116, v5, s[10:11] offset:2620
	global_store_dword v117, v6, s[10:11] offset:256
	global_store_dword v117, v7, s[10:11] offset:1044
	global_store_dword v117, v8, s[10:11] offset:1832
	global_store_dword v117, v9, s[10:11] offset:2620
	global_store_dword v118, v10, s[10:11] offset:256
	global_store_dword v118, v11, s[10:11] offset:1044
	global_store_dword v118, v12, s[10:11] offset:1832
	global_store_dword v118, v13, s[10:11] offset:2620
	global_store_dword v119, v14, s[10:11] offset:256
	global_store_dword v119, v15, s[10:11] offset:1044
	global_store_dword v119, v16, s[10:11] offset:1832
	global_store_dword v119, v17, s[10:11] offset:2620
	ds_read_b128 v[66:69], v112 offset:18432
	ds_read_b128 v[70:73], v112 offset:18464
	s_waitcnt lgkmcnt(1)
	v_mfma_f32_32x32x16_f16 v[2:17], v[74:77], v[66:69], 0
	ds_read_b128 v[66:69], v112 offset:18496
	s_waitcnt lgkmcnt(1)
	v_mfma_f32_32x32x16_f16 v[2:17], v[78:81], v[70:73], v[2:17]
	ds_read_b128 v[70:73], v112 offset:18528
	s_waitcnt lgkmcnt(1)
	v_mfma_f32_32x32x16_f16 v[2:17], v[82:85], v[66:69], v[2:17]
	s_waitcnt lgkmcnt(0)
	v_mfma_f32_32x32x16_f16 v[2:17], v[86:89], v[70:73], v[2:17]
	v_fma_f32 v120, v18, s16, -v90
	v_exp_f32_e32 v18, v120
	v_fma_f32 v121, v19, s16, -v91
	v_exp_f32_e32 v19, v121
	v_fma_f32 v122, v20, s16, -v92
	v_exp_f32_e32 v20, v122
	v_fma_f32 v123, v21, s16, -v93
	v_exp_f32_e32 v21, v123
	v_fma_f32 v120, v22, s16, -v94
	v_exp_f32_e32 v22, v120
	v_fma_f32 v121, v23, s16, -v95
	v_exp_f32_e32 v23, v121
	v_fma_f32 v122, v24, s16, -v96
	v_exp_f32_e32 v24, v122
	v_fma_f32 v123, v25, s16, -v97
	v_exp_f32_e32 v25, v123
	v_fma_f32 v120, v26, s16, -v98
	v_exp_f32_e32 v26, v120
	v_fma_f32 v121, v27, s16, -v99
	v_exp_f32_e32 v27, v121
	v_fma_f32 v122, v28, s16, -v100
	v_exp_f32_e32 v28, v122
	v_fma_f32 v123, v29, s16, -v101
	v_exp_f32_e32 v29, v123
	v_fma_f32 v120, v30, s16, -v102
	v_exp_f32_e32 v30, v120
	v_fma_f32 v121, v31, s16, -v103
	v_exp_f32_e32 v31, v121
	v_fma_f32 v122, v32, s16, -v104
	v_exp_f32_e32 v32, v122
	v_fma_f32 v123, v33, s16, -v105
	v_exp_f32_e32 v33, v123
	global_store_dword v116, v18, s[10:11] offset:384
	global_store_dword v116, v19, s[10:11] offset:1172
	global_store_dword v116, v20, s[10:11] offset:1960
	global_store_dword v116, v21, s[10:11] offset:2748
	global_store_dword v117, v22, s[10:11] offset:384
	global_store_dword v117, v23, s[10:11] offset:1172
	global_store_dword v117, v24, s[10:11] offset:1960
	global_store_dword v117, v25, s[10:11] offset:2748
	global_store_dword v118, v26, s[10:11] offset:384
	global_store_dword v118, v27, s[10:11] offset:1172
	global_store_dword v118, v28, s[10:11] offset:1960
	global_store_dword v118, v29, s[10:11] offset:2748
	global_store_dword v119, v30, s[10:11] offset:384
	global_store_dword v119, v31, s[10:11] offset:1172
	global_store_dword v119, v32, s[10:11] offset:1960
	global_store_dword v119, v33, s[10:11] offset:2748
	ds_read_b128 v[66:69], v112 offset:23040
	ds_read_b128 v[70:73], v112 offset:23072
	s_waitcnt lgkmcnt(1)
	v_mfma_f32_32x32x16_f16 v[18:33], v[74:77], v[66:69], 0
	ds_read_b128 v[66:69], v112 offset:23104
	s_waitcnt lgkmcnt(1)
	v_mfma_f32_32x32x16_f16 v[18:33], v[78:81], v[70:73], v[18:33]
	ds_read_b128 v[70:73], v112 offset:23136
	s_waitcnt lgkmcnt(1)
	v_mfma_f32_32x32x16_f16 v[18:33], v[82:85], v[66:69], v[18:33]
	s_waitcnt lgkmcnt(0)
	v_mfma_f32_32x32x16_f16 v[18:33], v[86:89], v[70:73], v[18:33]
	v_fma_f32 v120, v2, s16, -v90
	v_exp_f32_e32 v2, v120
	v_fma_f32 v121, v3, s16, -v91
	v_exp_f32_e32 v3, v121
	v_fma_f32 v122, v4, s16, -v92
	v_exp_f32_e32 v4, v122
	v_fma_f32 v123, v5, s16, -v93
	v_exp_f32_e32 v5, v123
	v_fma_f32 v120, v6, s16, -v94
	v_exp_f32_e32 v6, v120
	v_fma_f32 v121, v7, s16, -v95
	v_exp_f32_e32 v7, v121
	v_fma_f32 v122, v8, s16, -v96
	v_exp_f32_e32 v8, v122
	v_fma_f32 v123, v9, s16, -v97
	v_exp_f32_e32 v9, v123
	v_fma_f32 v120, v10, s16, -v98
	v_exp_f32_e32 v10, v120
	v_fma_f32 v121, v11, s16, -v99
	v_exp_f32_e32 v11, v121
	v_fma_f32 v122, v12, s16, -v100
	v_exp_f32_e32 v12, v122
	v_fma_f32 v123, v13, s16, -v101
	v_exp_f32_e32 v13, v123
	v_fma_f32 v120, v14, s16, -v102
	v_exp_f32_e32 v14, v120
	v_fma_f32 v121, v15, s16, -v103
	v_exp_f32_e32 v15, v121
	v_fma_f32 v122, v16, s16, -v104
	v_exp_f32_e32 v16, v122
	v_fma_f32 v123, v17, s16, -v105
	v_exp_f32_e32 v17, v123
	global_store_dword v116, v2, s[10:11] offset:512
	global_store_dword v116, v3, s[10:11] offset:1300
	global_store_dword v116, v4, s[10:11] offset:2088
	global_store_dword v116, v5, s[10:11] offset:2876
	global_store_dword v117, v6, s[10:11] offset:512
	global_store_dword v117, v7, s[10:11] offset:1300
	global_store_dword v117, v8, s[10:11] offset:2088
	global_store_dword v117, v9, s[10:11] offset:2876
	global_store_dword v118, v10, s[10:11] offset:512
	global_store_dword v118, v11, s[10:11] offset:1300
	global_store_dword v118, v12, s[10:11] offset:2088
	global_store_dword v118, v13, s[10:11] offset:2876
	global_store_dword v119, v14, s[10:11] offset:512
	global_store_dword v119, v15, s[10:11] offset:1300
	global_store_dword v119, v16, s[10:11] offset:2088
	global_store_dword v119, v17, s[10:11] offset:2876
	ds_read_b128 v[66:69], v112 offset:27648
	ds_read_b128 v[70:73], v112 offset:27680
	s_waitcnt lgkmcnt(1)
	v_mfma_f32_32x32x16_f16 v[2:17], v[74:77], v[66:69], 0
	ds_read_b128 v[66:69], v112 offset:27712
	s_waitcnt lgkmcnt(1)
	v_mfma_f32_32x32x16_f16 v[2:17], v[78:81], v[70:73], v[2:17]
	ds_read_b128 v[70:73], v112 offset:27744
	s_waitcnt lgkmcnt(1)
	v_mfma_f32_32x32x16_f16 v[2:17], v[82:85], v[66:69], v[2:17]
	s_waitcnt lgkmcnt(0)
	v_mfma_f32_32x32x16_f16 v[2:17], v[86:89], v[70:73], v[2:17]
	v_fma_f32 v120, v18, s16, -v90
	v_exp_f32_e32 v18, v120
	v_fma_f32 v121, v19, s16, -v91
	v_exp_f32_e32 v19, v121
	v_fma_f32 v122, v20, s16, -v92
	v_exp_f32_e32 v20, v122
	v_fma_f32 v123, v21, s16, -v93
	v_exp_f32_e32 v21, v123
	v_fma_f32 v120, v22, s16, -v94
	v_exp_f32_e32 v22, v120
	v_fma_f32 v121, v23, s16, -v95
	v_exp_f32_e32 v23, v121
	v_fma_f32 v122, v24, s16, -v96
	v_exp_f32_e32 v24, v122
	v_fma_f32 v123, v25, s16, -v97
	v_exp_f32_e32 v25, v123
	v_fma_f32 v120, v26, s16, -v98
	v_exp_f32_e32 v26, v120
	v_fma_f32 v121, v27, s16, -v99
	v_exp_f32_e32 v27, v121
	v_fma_f32 v122, v28, s16, -v100
	v_exp_f32_e32 v28, v122
	v_fma_f32 v123, v29, s16, -v101
	v_exp_f32_e32 v29, v123
	v_fma_f32 v120, v30, s16, -v102
	v_exp_f32_e32 v30, v120
	v_fma_f32 v121, v31, s16, -v103
	v_exp_f32_e32 v31, v121
	v_fma_f32 v122, v32, s16, -v104
	v_exp_f32_e32 v32, v122
	v_fma_f32 v123, v33, s16, -v105
	v_exp_f32_e32 v33, v123
	global_store_dword v116, v18, s[10:11] offset:640
	global_store_dword v116, v19, s[10:11] offset:1428
	global_store_dword v116, v20, s[10:11] offset:2216
	global_store_dword v116, v21, s[10:11] offset:3004
	global_store_dword v117, v22, s[10:11] offset:640
	global_store_dword v117, v23, s[10:11] offset:1428
	global_store_dword v117, v24, s[10:11] offset:2216
	global_store_dword v117, v25, s[10:11] offset:3004
	global_store_dword v118, v26, s[10:11] offset:640
	global_store_dword v118, v27, s[10:11] offset:1428
	global_store_dword v118, v28, s[10:11] offset:2216
	global_store_dword v118, v29, s[10:11] offset:3004
	global_store_dword v119, v30, s[10:11] offset:640
	global_store_dword v119, v31, s[10:11] offset:1428
	global_store_dword v119, v32, s[10:11] offset:2216
	global_store_dword v119, v33, s[10:11] offset:3004
	s_nop 15
	s_nop 1
	v_fma_f32 v120, v2, s16, -v90
	v_exp_f32_e32 v2, v120
	v_fma_f32 v121, v3, s16, -v91
	v_exp_f32_e32 v3, v121
	v_fma_f32 v122, v4, s16, -v92
	v_exp_f32_e32 v4, v122
	v_fma_f32 v123, v5, s16, -v93
	v_exp_f32_e32 v5, v123
	v_fma_f32 v120, v6, s16, -v94
	v_exp_f32_e32 v6, v120
	v_fma_f32 v121, v7, s16, -v95
	v_exp_f32_e32 v7, v121
	v_fma_f32 v122, v8, s16, -v96
	v_exp_f32_e32 v8, v122
	v_fma_f32 v123, v9, s16, -v97
	v_exp_f32_e32 v9, v123
	v_fma_f32 v120, v10, s16, -v98
	v_exp_f32_e32 v10, v120
	v_fma_f32 v121, v11, s16, -v99
	v_exp_f32_e32 v11, v121
	v_fma_f32 v122, v12, s16, -v100
	v_exp_f32_e32 v12, v122
	v_fma_f32 v123, v13, s16, -v101
	v_exp_f32_e32 v13, v123
	v_fma_f32 v120, v14, s16, -v102
	v_exp_f32_e32 v14, v120
	v_fma_f32 v121, v15, s16, -v103
	v_exp_f32_e32 v15, v121
	v_fma_f32 v122, v16, s16, -v104
	v_exp_f32_e32 v16, v122
	v_fma_f32 v123, v17, s16, -v105
	v_exp_f32_e32 v17, v123
	s_and_b64 exec, exec, s[22:23]
	global_store_dword v116, v2, s[10:11] offset:768
	global_store_dword v116, v3, s[10:11] offset:1556
	global_store_dword v116, v4, s[10:11] offset:2344
	global_store_dword v116, v5, s[10:11] offset:3132
	global_store_dword v117, v6, s[10:11] offset:768
	global_store_dword v117, v7, s[10:11] offset:1556
	global_store_dword v117, v8, s[10:11] offset:2344
	global_store_dword v117, v9, s[10:11] offset:3132
	global_store_dword v118, v10, s[10:11] offset:768
	global_store_dword v118, v11, s[10:11] offset:1556
	global_store_dword v118, v12, s[10:11] offset:2344
	global_store_dword v118, v13, s[10:11] offset:3132
	global_store_dword v119, v14, s[10:11] offset:768
	global_store_dword v119, v15, s[10:11] offset:1556
	global_store_dword v119, v16, s[10:11] offset:2344
	global_store_dword v119, v17, s[10:11] offset:3132
	s_mov_b64 exec, s[18:19]
	s_endpgm
